# combo: skip wout(b0)->inproj(b1) grid barrier; publish XGEN before leader acquire; FFN act stores nt sc1
# baseline (speedup 1.0000x reference)
; __device__ __forceinline__ unsigned xb_ld(unsigned* p)              { return __hip_atomic_load(p, __ATOMIC_RELAXED, __HIP_MEMORY_SCOPE_AGENT); }
; __device__ __forceinline__ unsigned xb_add(unsigned* p, unsigned v) { return __hip_atomic_fetch_add(p, v, __ATOMIC_RELAXED, __HIP_MEMORY_SCOPE_AGENT); }
; #define XB_SPIN(cond, bar) do { unsigned _sp = 0; while (cond) { __builtin_amdgcn_s_sleep(1); \
;     if ((++_sp & 255u) == 0u) { if (xb_ld(&(bar)[XB_TMO])) break; if (_sp > XB_SPIN_CAP) { atomicAdd(&(bar)[XB_TMO], 1u); break; } } } } while (0)
; __device__ __forceinline__ void xcd_barrier(const XcdBarrier& b) {
;     ...
;         const unsigned old = xb_add(&bar[XB_XSUB(b.x)], 1u);
;         const unsigned gen = old / nloc;
;         if (old + 1u == (gen + 1u) * nloc) {
;             __builtin_amdgcn_fence(__ATOMIC_RELEASE, "agent");
;             asm volatile("s_waitcnt vmcnt(0)" ::: "memory");
;             const unsigned og = xb_add(&bar[XB_TOP], 1u);
;             const unsigned tg = og / nx;
;             if (og + 1u == (tg + 1u) * nx) xb_add(&bar[XB_TOPGEN], 1u);
;             else XB_SPIN(xb_ld(&bar[XB_TOPGEN]) == tg, bar);
;             __builtin_amdgcn_fence(__ATOMIC_ACQUIRE, "agent");
;             xb_add(&bar[XB_XGEN(b.x)], 1u);
;             asm volatile("s_waitcnt vmcnt(0)" ::: "memory");
.LBB0_73:
	s_or_b64 exec, exec, s[6:7]
	v_mov_b32_e32 v1, 0x2000
	v_mov_b32_e32 v2, 1
	s_waitcnt vmcnt(0)
	global_atomic_add v1, v2, s[4:5] offset:1024
	buffer_inv sc1
	s_waitcnt vmcnt(0)

; __device__ __forceinline__ unsigned xb_ld(unsigned* p)              { return __hip_atomic_load(p, __ATOMIC_RELAXED, __HIP_MEMORY_SCOPE_AGENT); }
; __device__ __forceinline__ unsigned xb_add(unsigned* p, unsigned v) { return __hip_atomic_fetch_add(p, v, __ATOMIC_RELAXED, __HIP_MEMORY_SCOPE_AGENT); }
; #define XB_SPIN(cond, bar) do { unsigned _sp = 0; while (cond) { __builtin_amdgcn_s_sleep(1); \
;     if ((++_sp & 255u) == 0u) { if (xb_ld(&(bar)[XB_TMO])) break; if (_sp > XB_SPIN_CAP) { atomicAdd(&(bar)[XB_TMO], 1u); break; } } } } while (0)
; __device__ __forceinline__ void xcd_barrier(const XcdBarrier& b) {
;     ...
;         const unsigned old = xb_add(&bar[XB_XSUB(b.x)], 1u);
;         const unsigned gen = old / nloc;
;         if (old + 1u == (gen + 1u) * nloc) {
;             __builtin_amdgcn_fence(__ATOMIC_RELEASE, "agent");
;             asm volatile("s_waitcnt vmcnt(0)" ::: "memory");
;             const unsigned og = xb_add(&bar[XB_TOP], 1u);
;             const unsigned tg = og / nx;
;             if (og + 1u == (tg + 1u) * nx) xb_add(&bar[XB_TOPGEN], 1u);
;             else XB_SPIN(xb_ld(&bar[XB_TOPGEN]) == tg, bar);
;             __builtin_amdgcn_fence(__ATOMIC_ACQUIRE, "agent");
;             xb_add(&bar[XB_XGEN(b.x)], 1u);
;             asm volatile("s_waitcnt vmcnt(0)" ::: "memory");
.LBB0_76:
	s_or_b64 exec, exec, s[2:3]
	v_readlane_b32 s2, v252, 3
	v_readlane_b32 s3, v252, 4
	v_mov_b32_e32 v0, 1
	s_waitcnt vmcnt(0)
	s_nop 2
	global_atomic_add v1, v0, s[2:3]
	buffer_inv sc1
	s_waitcnt vmcnt(0)

; #define PG8_STAGE(bufoff, gbase, voff) do { _Pragma("unroll") for (int _i = 0; _i < 2; ++_i) \
;         __builtin_amdgcn_global_load_lds((const unsigned*)((const char*)(gbase) + (voff)[_i]), (LAS unsigned*)(lds + (bufoff) + ldsw + _i * 8192), 16, 0, 0); } while (0)
; #define PG8_LDA(dst, b, h) do { _Pragma("unroll") for (int m = 0; m < 4; ++m) _Pragma("unroll") for (int k = 0; k < 2; ++k) dst[m][k] = *(const LAS bf16x8*)(lds + PG8_SA(b, h) + aoff + m * 2048 + k * 1024); } while (0)
; #define PG8_LDB(dst, b, h) do { _Pragma("unroll") for (int n = 0; n < 2; ++n) _Pragma("unroll") for (int k = 0; k < 2; ++k) dst[n][k] = *(const LAS bf16x8*)(lds + PG8_SB(b, h) + boff + n * 2048 + k * 1024); } while (0)
; #define PG8_MMA(ai, bj, At, Bt) do { __builtin_amdgcn_s_setprio(1); _Pragma("unroll") for (int m = 0; m < 4; ++m) _Pragma("unroll") for (int n = 0; n < 2; ++n) _Pragma("unroll") for (int k = 0; k < 2; ++k) \
;         acc[ai][bj][m][n] = __builtin_amdgcn_mfma_f32_16x16x32_bf16(Bt[n][k], At[m][k], acc[ai][bj][m][n], 0, 0, 0); __builtin_amdgcn_s_setprio(0); } while (0)
; #define PG8_WAIT_V(n) asm volatile("s_waitcnt vmcnt(" #n ")" ::: "memory")
; #define PG8_WAIT_L(n) asm volatile("s_waitcnt lgkmcnt(" #n ")" ::: "memory")
; #define PG8_BAR __builtin_amdgcn_s_barrier()
; #define PG8_SCHED __builtin_amdgcn_sched_barrier(0)
; template <class Epi>
; __device__ __forceinline__ void gemm_phase(LAS unsigned char* lds, const int tid, const Gemm g, const Sched& S, const Epi& E) {
;     ...
;             PG8_LDB(B0, 0, 0); PG8_SCHED; PG8_LDA(At, 0, 0); PG8_STAGE(PG8_SA(1, 1), a1 + hstepA, voffA);
;             PG8_WAIT_L(8); PG8_BAR; PG8_WAIT_L(0); PG8_MMA(0, 0, At, B0); PG8_BAR; PG8_SCHED;
;             PG8_LDB(B1, 0, 1); PG8_STAGE(PG8_SB(0, 0), b2, voffB);
;             PG8_BAR; PG8_WAIT_L(0); PG8_MMA(0, 1, At, B1); PG8_BAR;
;             PG8_LDA(At, 0, 1); PG8_STAGE(PG8_SA(0, 0), a2, voffA);
;             PG8_BAR; PG8_WAIT_L(0); PG8_MMA(1, 0, At, B0); PG8_BAR; PG8_SCHED;
;             PG8_STAGE(PG8_SB(0, 1), b2 + hstepB, voffB);
;             PG8_WAIT_V(6); PG8_BAR; PG8_MMA(1, 1, At, B1); PG8_BAR;
.LBB0_1604:
	s_add_u32 s8, s2, 0xfffc0080
	s_addc_u32 s9, s3, -1
	s_add_i32 s52, 0, 0x10000
	v_add_u32_e32 v142, s52, v159
	ds_read_b128 v[130:133], v142
	ds_read_b128 v[134:137], v142 offset:1024
	ds_read_b128 v[138:141], v142 offset:2048
	ds_read_b128 v[142:145], v142 offset:3072
	s_cmp_eq_u32 s51, 12
	s_cselect_b32 s11, s42, s9
	s_cselect_b32 s10, s46, s8
	s_cselect_b32 s9, s47, s50
	s_cselect_b32 s8, s48, s49
	v_lshl_add_u64 v[160:161], s[2:3], 0, v[152:153]
	s_add_i32 m0, s16, 0xc000
	ds_read_b128 v[166:169], v165
	ds_read_b128 v[170:173], v165 offset:1024
	ds_read_b128 v[174:177], v165 offset:2048
	ds_read_b128 v[178:181], v165 offset:3072
	ds_read_b128 v[182:185], v165 offset:4096
	ds_read_b128 v[196:199], v165 offset:5120
	ds_read_b128 v[200:203], v165 offset:6144
	ds_read_b128 v[204:207], v165 offset:7168
	global_load_lds_dwordx4 v[160:161], off
	v_lshl_add_u64 v[160:161], s[2:3], 0, v[154:155]
	s_add_i32 m0, s16, 0xe000
	s_nop 0
	global_load_lds_dwordx4 v[160:161], off
	s_waitcnt lgkmcnt(8)
	s_barrier
	s_waitcnt lgkmcnt(0)
	s_setprio 1
	s_waitcnt lgkmcnt(0)
	v_mfma_f32_16x16x32_bf16 v[126:129], v[130:133], v[166:169], v[126:129]
	v_mfma_f32_16x16x32_bf16 v[118:121], v[138:141], v[166:169], v[118:121]
	v_mfma_f32_16x16x32_bf16 v[110:113], v[130:133], v[174:177], v[110:113]
	v_mfma_f32_16x16x32_bf16 v[102:105], v[138:141], v[174:177], v[102:105]
	v_mfma_f32_16x16x32_bf16 v[94:97], v[130:133], v[182:185], v[94:97]
	v_mfma_f32_16x16x32_bf16 v[86:89], v[138:141], v[182:185], v[86:89]
	v_mfma_f32_16x16x32_bf16 v[78:81], v[130:133], v[200:203], v[78:81]
	v_mfma_f32_16x16x32_bf16 v[70:73], v[138:141], v[200:203], v[70:73]
	v_mfma_f32_16x16x32_bf16 v[126:129], v[134:137], v[170:173], v[126:129]
	v_mfma_f32_16x16x32_bf16 v[118:121], v[142:145], v[170:173], v[118:121]
	v_mfma_f32_16x16x32_bf16 v[110:113], v[134:137], v[178:181], v[110:113]
	v_mfma_f32_16x16x32_bf16 v[102:105], v[142:145], v[178:181], v[102:105]
	v_mfma_f32_16x16x32_bf16 v[94:97], v[134:137], v[196:199], v[94:97]
	v_mfma_f32_16x16x32_bf16 v[86:89], v[142:145], v[196:199], v[86:89]
	v_mfma_f32_16x16x32_bf16 v[78:81], v[134:137], v[204:207], v[78:81]
	v_mfma_f32_16x16x32_bf16 v[70:73], v[142:145], v[204:207], v[70:73]
	s_setprio 0
	s_barrier
	s_add_i32 s54, 0, 0x14000
	s_add_i32 s52, s52, s14
	v_add_u32_e32 v156, s54, v159
	v_lshl_add_u64 v[160:161], s[8:9], 0, v[0:1]
	s_mov_b32 m0, s52
	ds_read_b128 v[208:211], v156
	ds_read_b128 v[212:215], v156 offset:1024
	ds_read_b128 v[216:219], v156 offset:2048
	ds_read_b128 v[220:223], v156 offset:3072
	global_load_lds_dwordx4 v[160:161], off
	v_lshl_add_u64 v[192:193], s[8:9], 0, v[146:147]
	s_add_i32 m0, s52, 0x2000
	s_nop 0
	global_load_lds_dwordx4 v[192:193], off
	s_barrier
	s_waitcnt lgkmcnt(0)
	s_setprio 1
	s_waitcnt lgkmcnt(0)
	v_mfma_f32_16x16x32_bf16 v[122:125], v[208:211], v[166:169], v[122:125]
	v_mfma_f32_16x16x32_bf16 v[114:117], v[216:219], v[166:169], v[114:117]
	v_mfma_f32_16x16x32_bf16 v[106:109], v[208:211], v[174:177], v[106:109]
	v_mfma_f32_16x16x32_bf16 v[98:101], v[216:219], v[174:177], v[98:101]
	v_mfma_f32_16x16x32_bf16 v[90:93], v[208:211], v[182:185], v[90:93]
	v_mfma_f32_16x16x32_bf16 v[82:85], v[216:219], v[182:185], v[82:85]
	v_mfma_f32_16x16x32_bf16 v[74:77], v[208:211], v[200:203], v[74:77]
	v_mfma_f32_16x16x32_bf16 v[66:69], v[216:219], v[200:203], v[66:69]
	v_mfma_f32_16x16x32_bf16 v[122:125], v[212:215], v[170:173], v[122:125]
	v_mfma_f32_16x16x32_bf16 v[114:117], v[220:223], v[170:173], v[114:117]
	v_mfma_f32_16x16x32_bf16 v[106:109], v[212:215], v[178:181], v[106:109]
	v_mfma_f32_16x16x32_bf16 v[98:101], v[220:223], v[178:181], v[98:101]
	v_mfma_f32_16x16x32_bf16 v[90:93], v[212:215], v[196:199], v[90:93]
	v_mfma_f32_16x16x32_bf16 v[82:85], v[220:223], v[196:199], v[82:85]
	v_mfma_f32_16x16x32_bf16 v[74:77], v[212:215], v[204:207], v[74:77]
	v_mfma_f32_16x16x32_bf16 v[66:69], v[220:223], v[204:207], v[66:69]
	s_setprio 0
	s_mov_b32 m0, s16
	v_lshl_add_u64 v[224:225], s[10:11], 0, v[150:151]
	s_barrier
	ds_read_b128 v[166:169], v165 offset:16384
	ds_read_b128 v[170:173], v165 offset:17408
	ds_read_b128 v[174:177], v165 offset:18432
	ds_read_b128 v[178:181], v165 offset:19456
	ds_read_b128 v[182:185], v165 offset:20480
	ds_read_b128 v[196:199], v165 offset:21504
	ds_read_b128 v[200:203], v165 offset:22528
	ds_read_b128 v[204:207], v165 offset:23552
	global_load_lds_dwordx4 v[224:225], off
	v_lshl_add_u64 v[226:227], s[10:11], 0, v[148:149]
	s_mov_b32 m0, s17
	s_nop 0
	global_load_lds_dwordx4 v[226:227], off
	s_barrier
	s_waitcnt lgkmcnt(0)
	s_setprio 1
	s_waitcnt lgkmcnt(0)
	v_mfma_f32_16x16x32_bf16 v[62:65], v[130:133], v[166:169], v[62:65]
	v_mfma_f32_16x16x32_bf16 v[54:57], v[138:141], v[166:169], v[54:57]
	v_mfma_f32_16x16x32_bf16 v[46:49], v[130:133], v[174:177], v[46:49]
	v_mfma_f32_16x16x32_bf16 v[38:41], v[138:141], v[174:177], v[38:41]
	v_mfma_f32_16x16x32_bf16 v[30:33], v[130:133], v[182:185], v[30:33]
	v_mfma_f32_16x16x32_bf16 v[22:25], v[138:141], v[182:185], v[22:25]
	v_mfma_f32_16x16x32_bf16 v[14:17], v[130:133], v[200:203], v[14:17]
	v_mfma_f32_16x16x32_bf16 v[6:9], v[138:141], v[200:203], v[6:9]
	v_mfma_f32_16x16x32_bf16 v[62:65], v[134:137], v[170:173], v[62:65]
	v_mfma_f32_16x16x32_bf16 v[54:57], v[142:145], v[170:173], v[54:57]
	v_mfma_f32_16x16x32_bf16 v[46:49], v[134:137], v[178:181], v[46:49]
	v_mfma_f32_16x16x32_bf16 v[38:41], v[142:145], v[178:181], v[38:41]
	v_mfma_f32_16x16x32_bf16 v[30:33], v[134:137], v[196:199], v[30:33]
	v_mfma_f32_16x16x32_bf16 v[22:25], v[142:145], v[196:199], v[22:25]
	v_mfma_f32_16x16x32_bf16 v[14:17], v[134:137], v[204:207], v[14:17]
	v_mfma_f32_16x16x32_bf16 v[6:9], v[142:145], v[204:207], v[6:9]
	s_setprio 0
	s_barrier
; #define PG8_STAGE(bufoff, gbase, voff) do { _Pragma("unroll") for (int _i = 0; _i < 2; ++_i) \
;         __builtin_amdgcn_global_load_lds((const unsigned*)((const char*)(gbase) + (voff)[_i]), (LAS unsigned*)(lds + (bufoff) + ldsw + _i * 8192), 16, 0, 0); } while (0)
; #define PG8_LDA(dst, b, h) do { _Pragma("unroll") for (int m = 0; m < 4; ++m) _Pragma("unroll") for (int k = 0; k < 2; ++k) dst[m][k] = *(const LAS bf16x8*)(lds + PG8_SA(b, h) + aoff + m * 2048 + k * 1024); } while (0)
; #define PG8_LDB(dst, b, h) do { _Pragma("unroll") for (int n = 0; n < 2; ++n) _Pragma("unroll") for (int k = 0; k < 2; ++k) dst[n][k] = *(const LAS bf16x8*)(lds + PG8_SB(b, h) + boff + n * 2048 + k * 1024); } while (0)
; #define PG8_MMA(ai, bj, At, Bt) do { __builtin_amdgcn_s_setprio(1); _Pragma("unroll") for (int m = 0; m < 4; ++m) _Pragma("unroll") for (int n = 0; n < 2; ++n) _Pragma("unroll") for (int k = 0; k < 2; ++k) \
;         acc[ai][bj][m][n] = __builtin_amdgcn_mfma_f32_16x16x32_bf16(Bt[n][k], At[m][k], acc[ai][bj][m][n], 0, 0, 0); __builtin_amdgcn_s_setprio(0); } while (0)
; #define PG8_WAIT_V(n) asm volatile("s_waitcnt vmcnt(" #n ")" ::: "memory")
; #define PG8_WAIT_L(n) asm volatile("s_waitcnt lgkmcnt(" #n ")" ::: "memory")
; #define PG8_BAR __builtin_amdgcn_s_barrier()
; #define PG8_SCHED __builtin_amdgcn_sched_barrier(0)
; template <class Epi>
; __device__ __forceinline__ void gemm_phase(LAS unsigned char* lds, const int tid, const Gemm g, const Sched& S, const Epi& E) {
;     ...
;             PG8_WAIT_V(6); PG8_BAR; PG8_MMA(1, 1, At, B1); PG8_BAR;
;             PG8_LDB(B0, 1, 0); PG8_SCHED; PG8_LDA(At, 1, 0); PG8_STAGE(PG8_SA(0, 1), a2 + hstepA, voffA);
;             PG8_WAIT_L(8); PG8_BAR; PG8_WAIT_L(0); PG8_MMA(0, 0, At, B0); PG8_BAR; PG8_SCHED;
;             PG8_LDB(B1, 1, 1); PG8_STAGE(PG8_SB(1, 0), b3, voffB);
;             PG8_BAR; PG8_WAIT_L(0); PG8_MMA(0, 1, At, B1); PG8_BAR;
;             PG8_LDA(At, 1, 1); PG8_STAGE(PG8_SA(1, 0), a3, voffA);
;             PG8_BAR; PG8_WAIT_L(0); PG8_MMA(1, 0, At, B0); PG8_BAR; PG8_SCHED;
	s_add_u32 s52, s8, 0x40000
	s_addc_u32 s53, s9, 0
	s_add_i32 s54, s54, s14
	v_lshl_add_u64 v[130:131], s[52:53], 0, v[0:1]
	s_mov_b32 m0, s54
	s_nop 0
	global_load_lds_dwordx4 v[130:131], off
	v_lshl_add_u64 v[130:131], s[52:53], 0, v[146:147]
	s_add_i32 m0, s54, 0x2000
	s_nop 0
	global_load_lds_dwordx4 v[130:131], off
	s_waitcnt vmcnt(6)
	s_barrier
	s_setprio 1
	v_mfma_f32_16x16x32_bf16 v[58:61], v[208:211], v[166:169], v[58:61]
	v_mfma_f32_16x16x32_bf16 v[50:53], v[216:219], v[166:169], v[50:53]
	v_mfma_f32_16x16x32_bf16 v[42:45], v[208:211], v[174:177], v[42:45]
	v_mfma_f32_16x16x32_bf16 v[34:37], v[216:219], v[174:177], v[34:37]
	v_mfma_f32_16x16x32_bf16 v[26:29], v[208:211], v[182:185], v[26:29]
	v_mfma_f32_16x16x32_bf16 v[18:21], v[216:219], v[182:185], v[18:21]
	v_mfma_f32_16x16x32_bf16 v[10:13], v[208:211], v[200:203], v[10:13]
	v_mfma_f32_16x16x32_bf16 v[2:5], v[216:219], v[200:203], v[2:5]
	v_mfma_f32_16x16x32_bf16 v[58:61], v[212:215], v[170:173], v[58:61]
	v_mfma_f32_16x16x32_bf16 v[50:53], v[220:223], v[170:173], v[50:53]
	v_mfma_f32_16x16x32_bf16 v[42:45], v[212:215], v[178:181], v[42:45]
	v_mfma_f32_16x16x32_bf16 v[34:37], v[220:223], v[178:181], v[34:37]
	v_mfma_f32_16x16x32_bf16 v[26:29], v[212:215], v[196:199], v[26:29]
	v_mfma_f32_16x16x32_bf16 v[18:21], v[220:223], v[196:199], v[18:21]
	v_mfma_f32_16x16x32_bf16 v[10:13], v[212:215], v[204:207], v[10:13]
	v_mfma_f32_16x16x32_bf16 v[2:5], v[220:223], v[204:207], v[2:5]
	s_setprio 0
	s_add_i32 s52, 0, 0x18000
	v_add_u32_e32 v142, s52, v159
	s_barrier
	ds_read_b128 v[130:133], v142
	ds_read_b128 v[134:137], v142 offset:1024
	ds_read_b128 v[138:141], v142 offset:2048
	ds_read_b128 v[142:145], v142 offset:3072
	s_add_u32 s10, s10, 0x40000
	s_addc_u32 s11, s11, 0
	s_mov_b32 m0, s20
	v_lshl_add_u64 v[208:209], s[10:11], 0, v[150:151]
	ds_read_b128 v[166:169], v165 offset:32768
	ds_read_b128 v[170:173], v165 offset:33792
	ds_read_b128 v[174:177], v165 offset:34816
	ds_read_b128 v[178:181], v165 offset:35840
	ds_read_b128 v[182:185], v165 offset:36864
	ds_read_b128 v[196:199], v165 offset:37888
	ds_read_b128 v[200:203], v165 offset:38912
	ds_read_b128 v[204:207], v165 offset:39936
	global_load_lds_dwordx4 v[208:209], off
	v_lshl_add_u64 v[208:209], s[10:11], 0, v[148:149]
	s_mov_b32 m0, s21
	s_nop 0
	global_load_lds_dwordx4 v[208:209], off
	s_waitcnt lgkmcnt(8)
	s_barrier
	s_waitcnt lgkmcnt(0)
	s_setprio 1
	s_waitcnt lgkmcnt(0)
	v_mfma_f32_16x16x32_bf16 v[126:129], v[130:133], v[166:169], v[126:129]
	v_mfma_f32_16x16x32_bf16 v[118:121], v[138:141], v[166:169], v[118:121]
	v_mfma_f32_16x16x32_bf16 v[110:113], v[130:133], v[174:177], v[110:113]
	v_mfma_f32_16x16x32_bf16 v[102:105], v[138:141], v[174:177], v[102:105]
	v_mfma_f32_16x16x32_bf16 v[94:97], v[130:133], v[182:185], v[94:97]
	v_mfma_f32_16x16x32_bf16 v[86:89], v[138:141], v[182:185], v[86:89]
	v_mfma_f32_16x16x32_bf16 v[78:81], v[130:133], v[200:203], v[78:81]
	v_mfma_f32_16x16x32_bf16 v[70:73], v[138:141], v[200:203], v[70:73]
	v_mfma_f32_16x16x32_bf16 v[126:129], v[134:137], v[170:173], v[126:129]
	v_mfma_f32_16x16x32_bf16 v[118:121], v[142:145], v[170:173], v[118:121]
	v_mfma_f32_16x16x32_bf16 v[110:113], v[134:137], v[178:181], v[110:113]
	v_mfma_f32_16x16x32_bf16 v[102:105], v[142:145], v[178:181], v[102:105]
	v_mfma_f32_16x16x32_bf16 v[94:97], v[134:137], v[196:199], v[94:97]
	v_mfma_f32_16x16x32_bf16 v[86:89], v[142:145], v[196:199], v[86:89]
	v_mfma_f32_16x16x32_bf16 v[78:81], v[134:137], v[204:207], v[78:81]
	v_mfma_f32_16x16x32_bf16 v[70:73], v[142:145], v[204:207], v[70:73]
	s_setprio 0
	s_barrier
	s_add_i32 s10, 0, 0x1c000
	s_add_i32 s11, s52, s14
	v_add_u32_e32 v156, s10, v159
	v_lshl_add_u64 v[160:161], v[160:161], 0, s[44:45]
	s_mov_b32 m0, s11
	ds_read_b128 v[208:211], v156
	ds_read_b128 v[212:215], v156 offset:1024
	ds_read_b128 v[216:219], v156 offset:2048
	ds_read_b128 v[220:223], v156 offset:3072
	global_load_lds_dwordx4 v[160:161], off
	v_lshl_add_u64 v[160:161], v[192:193], 0, s[44:45]
	s_add_i32 m0, s11, 0x2000
	s_nop 0
	global_load_lds_dwordx4 v[160:161], off
	s_barrier
	s_waitcnt lgkmcnt(0)
	s_setprio 1
	s_waitcnt lgkmcnt(0)
	v_mfma_f32_16x16x32_bf16 v[122:125], v[208:211], v[166:169], v[122:125]
	v_mfma_f32_16x16x32_bf16 v[114:117], v[216:219], v[166:169], v[114:117]
	v_mfma_f32_16x16x32_bf16 v[106:109], v[208:211], v[174:177], v[106:109]
	v_mfma_f32_16x16x32_bf16 v[98:101], v[216:219], v[174:177], v[98:101]
	v_mfma_f32_16x16x32_bf16 v[90:93], v[208:211], v[182:185], v[90:93]
	v_mfma_f32_16x16x32_bf16 v[82:85], v[216:219], v[182:185], v[82:85]
	v_mfma_f32_16x16x32_bf16 v[74:77], v[208:211], v[200:203], v[74:77]
	v_mfma_f32_16x16x32_bf16 v[66:69], v[216:219], v[200:203], v[66:69]
	v_mfma_f32_16x16x32_bf16 v[122:125], v[212:215], v[170:173], v[122:125]
	v_mfma_f32_16x16x32_bf16 v[114:117], v[220:223], v[170:173], v[114:117]
	v_mfma_f32_16x16x32_bf16 v[106:109], v[212:215], v[178:181], v[106:109]
	v_mfma_f32_16x16x32_bf16 v[98:101], v[220:223], v[178:181], v[98:101]
	v_mfma_f32_16x16x32_bf16 v[90:93], v[212:215], v[196:199], v[90:93]
	v_mfma_f32_16x16x32_bf16 v[82:85], v[220:223], v[196:199], v[82:85]
	v_mfma_f32_16x16x32_bf16 v[74:77], v[212:215], v[204:207], v[74:77]
	v_mfma_f32_16x16x32_bf16 v[66:69], v[220:223], v[204:207], v[66:69]
	s_setprio 0
	s_mov_b32 m0, s26
	v_lshl_add_u64 v[160:161], v[224:225], 0, s[44:45]
	s_barrier
	ds_read_b128 v[166:169], v165 offset:49152
	ds_read_b128 v[170:173], v165 offset:50176
	ds_read_b128 v[174:177], v165 offset:51200
	ds_read_b128 v[178:181], v165 offset:52224
	ds_read_b128 v[182:185], v165 offset:53248
	ds_read_b128 v[196:199], v165 offset:54272
	ds_read_b128 v[200:203], v165 offset:55296
	ds_read_b128 v[204:207], v165 offset:56320
	global_load_lds_dwordx4 v[160:161], off
	v_lshl_add_u64 v[160:161], v[226:227], 0, s[44:45]
	s_mov_b32 m0, s27
	s_nop 0
	global_load_lds_dwordx4 v[160:161], off
	s_barrier
; #define PG8_STAGE(bufoff, gbase, voff) do { _Pragma("unroll") for (int _i = 0; _i < 2; ++_i) \
;         __builtin_amdgcn_global_load_lds((const unsigned*)((const char*)(gbase) + (voff)[_i]), (LAS unsigned*)(lds + (bufoff) + ldsw + _i * 8192), 16, 0, 0); } while (0)
; #define PG8_MMA(ai, bj, At, Bt) do { __builtin_amdgcn_s_setprio(1); _Pragma("unroll") for (int m = 0; m < 4; ++m) _Pragma("unroll") for (int n = 0; n < 2; ++n) _Pragma("unroll") for (int k = 0; k < 2; ++k) \
;         acc[ai][bj][m][n] = __builtin_amdgcn_mfma_f32_16x16x32_bf16(Bt[n][k], At[m][k], acc[ai][bj][m][n], 0, 0, 0); __builtin_amdgcn_s_setprio(0); } while (0)
; #define PG8_WAIT_V(n) asm volatile("s_waitcnt vmcnt(" #n ")" ::: "memory")
; #define PG8_BAR __builtin_amdgcn_s_barrier()
; template <class Epi>
; __device__ __forceinline__ void gemm_phase(LAS unsigned char* lds, const int tid, const Gemm g, const Sched& S, const Epi& E) {
;     ...
;             PG8_STAGE(PG8_SB(1, 1), b3 + hstepB, voffB);
;             PG8_WAIT_V(6); PG8_BAR; PG8_MMA(1, 1, At, B1); PG8_BAR;
;     __device__ __forceinline__ bool operator()(f32x4 (&acc)[2][2][4][2], const Unit& u, int wr, int wc, int fr, int fq) const {
;     ...
;         { f32x4 pq[2][4];
; #pragma unroll
;           for (int ai = 0; ai < 2; ++ai)
; #pragma unroll
;             for (int m = 0; m < 4; ++m) pq[ai][m] = *(const f32x4*)statp(ws, row0 + ai * HALF + m * 16, 1);
; #pragma unroll
;           for (int ai = 0; ai < 2; ++ai)
; #pragma unroll
;             for (int m = 0; m < 4; ++m) sv[ai][m] = rsqrtf(((pq[ai][m][0] + pq[ai][m][1]) + (pq[ai][m][2] + pq[ai][m][3])) * (1.0f / D) + NORM_EPS); }
	s_waitcnt lgkmcnt(0)
	s_setprio 1
	s_waitcnt lgkmcnt(0)
	v_mfma_f32_16x16x32_bf16 v[62:65], v[130:133], v[166:169], v[62:65]
	v_mfma_f32_16x16x32_bf16 v[54:57], v[138:141], v[166:169], v[54:57]
	v_mfma_f32_16x16x32_bf16 v[46:49], v[130:133], v[174:177], v[46:49]
	v_mfma_f32_16x16x32_bf16 v[38:41], v[138:141], v[174:177], v[38:41]
	v_mfma_f32_16x16x32_bf16 v[30:33], v[130:133], v[182:185], v[30:33]
	v_mfma_f32_16x16x32_bf16 v[22:25], v[138:141], v[182:185], v[22:25]
	v_mfma_f32_16x16x32_bf16 v[14:17], v[130:133], v[200:203], v[14:17]
	v_mfma_f32_16x16x32_bf16 v[6:9], v[138:141], v[200:203], v[6:9]
	v_mfma_f32_16x16x32_bf16 v[62:65], v[134:137], v[170:173], v[62:65]
	v_mfma_f32_16x16x32_bf16 v[54:57], v[142:145], v[170:173], v[54:57]
	v_mfma_f32_16x16x32_bf16 v[46:49], v[134:137], v[178:181], v[46:49]
	v_mfma_f32_16x16x32_bf16 v[38:41], v[142:145], v[178:181], v[38:41]
	v_mfma_f32_16x16x32_bf16 v[30:33], v[134:137], v[196:199], v[30:33]
	v_mfma_f32_16x16x32_bf16 v[22:25], v[142:145], v[196:199], v[22:25]
	v_mfma_f32_16x16x32_bf16 v[14:17], v[134:137], v[204:207], v[14:17]
	v_mfma_f32_16x16x32_bf16 v[6:9], v[142:145], v[204:207], v[6:9]
	s_setprio 0
	s_barrier
	s_add_u32 s8, s8, 0x40080
	s_addc_u32 s9, s9, 0
	s_add_i32 s10, s10, s14
	v_lshl_add_u64 v[130:131], s[8:9], 0, v[0:1]
	s_mov_b32 m0, s10
	s_nop 0
	global_load_lds_dwordx4 v[130:131], off
	v_lshl_add_u64 v[130:131], s[8:9], 0, v[146:147]
	s_add_i32 m0, s10, 0x2000
	s_nop 0
	global_load_lds_dwordx4 v[130:131], off
	s_waitcnt vmcnt(6)
	s_barrier
	s_setprio 1
	v_mfma_f32_16x16x32_bf16 v[58:61], v[208:211], v[166:169], v[58:61]
	v_mfma_f32_16x16x32_bf16 v[50:53], v[216:219], v[166:169], v[50:53]
	v_mfma_f32_16x16x32_bf16 v[42:45], v[208:211], v[174:177], v[42:45]
	v_mfma_f32_16x16x32_bf16 v[34:37], v[216:219], v[174:177], v[34:37]
	v_mfma_f32_16x16x32_bf16 v[26:29], v[208:211], v[182:185], v[26:29]
	v_mfma_f32_16x16x32_bf16 v[18:21], v[216:219], v[182:185], v[18:21]
	v_mfma_f32_16x16x32_bf16 v[10:13], v[208:211], v[200:203], v[10:13]
	v_mfma_f32_16x16x32_bf16 v[2:5], v[216:219], v[200:203], v[2:5]
	v_mfma_f32_16x16x32_bf16 v[58:61], v[212:215], v[170:173], v[58:61]
	v_mfma_f32_16x16x32_bf16 v[50:53], v[220:223], v[170:173], v[50:53]
	v_mfma_f32_16x16x32_bf16 v[42:45], v[212:215], v[178:181], v[42:45]
	v_mfma_f32_16x16x32_bf16 v[34:37], v[220:223], v[178:181], v[34:37]
	v_mfma_f32_16x16x32_bf16 v[26:29], v[212:215], v[196:199], v[26:29]
	v_mfma_f32_16x16x32_bf16 v[18:21], v[220:223], v[196:199], v[18:21]
	v_mfma_f32_16x16x32_bf16 v[10:13], v[212:215], v[204:207], v[10:13]
	v_mfma_f32_16x16x32_bf16 v[2:5], v[220:223], v[204:207], v[2:5]
	s_setprio 0
	s_add_i32 s51, s51, 2
	s_add_u32 s2, s2, 0x100
	s_addc_u32 s3, s3, 0
	s_add_u32 s49, s49, 0x100
	s_addc_u32 s50, s50, 0
	s_cmp_gt_u32 s51, 13
	s_barrier
	s_cbranch_scc0 .LBB0_1604
	v_lshl_add_u32 v160, s39, 8, v157
	v_readlane_b32 s2, v252, 16
	v_ashrrev_i32_e32 v161, 31, v160
	v_readlane_b32 s3, v252, 17
	v_or_b32_e32 v132, 16, v160
	v_ashrrev_i32_e32 v133, 31, v132
	v_lshl_add_u64 v[130:131], v[160:161], 4, s[2:3]
	global_load_dwordx4 v[170:173], v[130:131], off
	v_lshl_add_u64 v[132:133], v[132:133], 4, s[2:3]
	global_load_dwordx4 v[174:177], v[132:133], off
	v_or_b32_e32 v132, 32, v160
	v_ashrrev_i32_e32 v133, 31, v132
	v_lshl_add_u64 v[132:133], v[132:133], 4, s[2:3]
	global_load_dwordx4 v[178:181], v[132:133], off
	v_or_b32_e32 v132, 48, v160
	v_ashrrev_i32_e32 v133, 31, v132
	v_lshl_add_u64 v[132:133], v[132:133], 4, s[2:3]
	global_load_dwordx4 v[182:185], v[132:133], off
	global_load_dwordx4 v[142:145], v[130:131], off offset:2048
	global_load_dwordx4 v[138:141], v[130:131], off offset:2304
	global_load_dwordx4 v[134:137], v[130:131], off offset:2560
	s_nop 0
	global_load_dwordx4 v[130:133], v[130:131], off offset:2816
	s_mov_b32 s2, 0x358637bd
	s_mov_b32 s8, 0x3a800000
	v_lshl_or_b32 v168, s22, 7, v163
	s_mov_b32 s22, s29
	s_mov_b32 s39, s38
	s_waitcnt vmcnt(0)
	v_mov_b32_e32 v166, v171
	v_mov_b32_e32 v167, v172
	v_mov_b32_e32 v171, v173
	v_pk_add_f32 v[166:167], v[166:167], v[170:171]
	v_mov_b32_e32 v170, v175
	v_mov_b32_e32 v171, v176
	v_mov_b32_e32 v175, v177
	v_pk_add_f32 v[170:171], v[170:171], v[174:175]
	v_mov_b32_e32 v173, v166
	v_mov_b32_e32 v172, v170
	v_mov_b32_e32 v166, v171
	v_pk_add_f32 v[170:171], v[172:173], v[166:167]
	v_mov_b64_e32 v[166:167], s[2:3]
	v_pk_fma_f32 v[170:171], v[170:171], s[8:9], v[166:167] op_sel_hi:[1,0,0]
	v_mov_b32_e32 v172, v183
	v_mul_f32_e32 v156, 0x4b800000, v171
	v_cmp_gt_f32_e64 s[2:3], s33, v171
	v_cmp_gt_f32_e32 vcc, s33, v170
	v_mov_b32_e32 v173, v184
	v_cndmask_b32_e64 v156, v171, v156, s[2:3]
	v_rsq_f32_e32 v156, v156
	v_mov_b32_e32 v171, v180
	v_mov_b32_e32 v183, v185
	v_pk_add_f32 v[172:173], v[172:173], v[182:183]
	v_mul_f32_e32 v158, 0x45800000, v156
	v_cndmask_b32_e64 v164, v156, v158, s[2:3]
	v_mul_f32_e32 v156, 0x4b800000, v170
	v_cndmask_b32_e32 v156, v170, v156, vcc
	v_rsq_f32_e32 v156, v156
	v_mov_b32_e32 v170, v179
	v_mov_b32_e32 v179, v181
	v_pk_add_f32 v[170:171], v[170:171], v[178:179]
	v_mov_b32_e32 v174, v172
	v_mov_b32_e32 v175, v170
	v_mov_b32_e32 v170, v173
	v_pk_add_f32 v[170:171], v[174:175], v[170:171]
	v_mul_f32_e32 v158, 0x45800000, v156
	v_pk_fma_f32 v[170:171], v[170:171], s[8:9], v[166:167] op_sel_hi:[1,0,0]
	v_cndmask_b32_e32 v162, v156, v158, vcc
	v_mul_f32_e32 v156, 0x4b800000, v171
	v_cmp_gt_f32_e64 s[2:3], s33, v171
	v_cmp_gt_f32_e32 vcc, s33, v170
	v_pk_mul_f32 v[126:127], v[126:127], v[164:165] op_sel_hi:[1,0]
	v_cndmask_b32_e64 v156, v171, v156, s[2:3]
	v_rsq_f32_e32 v156, v156
	v_mov_b32_e32 v171, v144
	v_mov_b32_e32 v144, v139
	v_mov_b32_e32 v139, v141
; __device__ __forceinline__ unsigned pk2(float lo, float hi) { const f32x2 f = {lo, hi}; const bf16n2 v = __builtin_convertvector(f, bf16n2); return __builtin_bit_cast(unsigned, v); }
; __device__ __forceinline__ float sigmoidf_(float x) { return __builtin_amdgcn_rcpf(1.0f + __expf(-x)); }
;     __device__ __forceinline__ bool operator()(f32x4 (&acc)[2][2][4][2], const Unit& u, int wr, int wc, int fr, int fq) const {
;     ...
;             for (int m = 0; m < 4; ++m) sv[ai][m] = rsqrtf(((pq[ai][m][0] + pq[ai][m][1]) + (pq[ai][m][2] + pq[ai][m][3])) * (1.0f / D) + NORM_EPS); }
; #pragma unroll
;         for (int ai = 0; ai < 2; ++ai)
; #pragma unroll
;             for (int m = 0; m < 4; ++m) { const int row = row0 + ai * HALF + m * 16;
;                 const float s = sv[ai][m];
;                 float o[8];
; #pragma unroll
;                 for (int n = 0; n < 2; ++n)
; #pragma unroll
;                     for (int j = 0; j < 4; ++j) { const float gg = acc[ai][0][m][n][j] * s, uu = acc[ai][1][m][n][j] * s; o[n * 4 + j] = gg * sigmoidf_(gg) * uu; }
;                 u32x4 w; w.x = pk2(o[0], o[1]); w.y = pk2(o[2], o[3]); w.z = pk2(o[4], o[5]); w.w = pk2(o[6], o[7]);
;                 __builtin_amdgcn_raw_buffer_store_b128(w, rs_act, ((unsigned)row * (unsigned)FFN + (unsigned)col0) * 2u, 0, 0); }
	v_mul_f32_e32 v158, 0x45800000, v156
	v_cndmask_b32_e64 v158, v156, v158, s[2:3]
	v_mul_f32_e32 v156, 0x4b800000, v170
	v_cndmask_b32_e32 v156, v170, v156, vcc
	v_mov_b32_e32 v170, v143
	v_mov_b32_e32 v143, v145
	v_mov_b32_e32 v145, v140
	v_pk_add_f32 v[142:143], v[170:171], v[142:143]
	v_pk_add_f32 v[138:139], v[144:145], v[138:139]
	v_mov_b32_e32 v141, v142
	v_mov_b32_e32 v140, v138
	v_mov_b32_e32 v142, v139
	v_pk_add_f32 v[138:139], v[140:141], v[142:143]
	v_rsq_f32_e32 v156, v156
	v_pk_fma_f32 v[138:139], v[138:139], s[8:9], v[166:167] op_sel_hi:[1,0,0]
	v_mov_b32_e32 v142, v135
	v_mul_f32_e32 v140, 0x4b800000, v139
	v_cmp_gt_f32_e64 s[2:3], s33, v139
	v_mov_b32_e32 v143, v136
	v_mov_b32_e32 v135, v137
	v_cndmask_b32_e64 v139, v139, v140, s[2:3]
	v_rsq_f32_e32 v139, v139
	v_mov_b32_e32 v136, v131
	v_mov_b32_e32 v137, v132
	v_mov_b32_e32 v131, v133
	v_pk_add_f32 v[134:135], v[142:143], v[134:135]
	v_pk_add_f32 v[130:131], v[136:137], v[130:131]
	v_mov_b32_e32 v133, v134
	v_mov_b32_e32 v132, v130
	v_mov_b32_e32 v134, v131
	v_pk_add_f32 v[130:131], v[132:133], v[134:135]
	v_mul_f32_e32 v161, 0x45800000, v156
	v_mul_f32_e32 v140, 0x45800000, v139
	v_pk_fma_f32 v[130:131], v[130:131], s[8:9], v[166:167] op_sel_hi:[1,0,0]
	v_cndmask_b32_e32 v156, v156, v161, vcc
	v_cmp_gt_f32_e32 vcc, s33, v138
	v_cndmask_b32_e64 v140, v139, v140, s[2:3]
	v_mul_f32_e32 v139, 0x4b800000, v138
	v_mul_f32_e32 v132, 0x4b800000, v131
	v_cmp_gt_f32_e64 s[2:3], s33, v131
	v_cndmask_b32_e32 v138, v138, v139, vcc
	v_rsq_f32_e32 v138, v138
	v_cndmask_b32_e64 v131, v131, v132, s[2:3]
	v_rsq_f32_e32 v131, v131
	v_pk_mul_f32 v[122:123], v[122:123], v[164:165] op_sel_hi:[1,0]
	v_mul_f32_e32 v139, 0x45800000, v138
	v_cndmask_b32_e32 v138, v138, v139, vcc
	v_mul_f32_e32 v132, 0x45800000, v131
	v_cmp_gt_f32_e32 vcc, s33, v130
	v_cndmask_b32_e64 v132, v131, v132, s[2:3]
	v_mul_f32_e32 v131, 0x4b800000, v130
	v_cndmask_b32_e32 v130, v130, v131, vcc
	v_rsq_f32_e32 v130, v130
	v_pk_mul_f32 v[124:125], v[124:125], v[164:165] op_sel_hi:[1,0]
	v_pk_mul_f32 v[118:119], v[118:119], v[164:165] op_sel_hi:[1,0]
	v_pk_mul_f32 v[114:115], v[114:115], v[164:165] op_sel_hi:[1,0]
	v_mul_f32_e32 v131, 0x45800000, v130
	v_cndmask_b32_e32 v130, v130, v131, vcc
	v_mul_f32_e32 v131, 0xbfb8aa3b, v126
	v_exp_f32_e32 v131, v131
	v_pk_mul_f32 v[116:117], v[116:117], v[164:165] op_sel_hi:[1,0]
	v_pk_mul_f32 v[110:111], v[110:111], v[162:163] op_sel_hi:[1,0]
	s_movk_i32 s2, 0xb00
	v_add_f32_e32 v131, 1.0, v131
	v_rcp_f32_e32 v134, v131
	v_mul_f32_e32 v131, 0xbfb8aa3b, v127
	v_exp_f32_e32 v131, v131
	v_readlane_b32 s8, v252, 41
	v_readlane_b32 s10, v252, 43
	v_readlane_b32 s11, v252, 44
	v_add_f32_e32 v131, 1.0, v131
	v_rcp_f32_e32 v135, v131
	v_readlane_b32 s9, v252, 42
	s_mov_b32 s10, s62
	s_mov_b32 s11, s63
	v_pk_mul_f32 v[126:127], v[126:127], v[134:135]
	v_pk_mul_f32 v[106:107], v[106:107], v[162:163] op_sel_hi:[1,0]
	v_pk_mul_f32 v[122:123], v[122:123], v[126:127]
	v_pk_mul_f32 v[126:127], v[128:129], v[164:165] op_sel_hi:[1,0]
	v_pk_mul_f32 v[108:109], v[108:109], v[162:163] op_sel_hi:[1,0]
	v_mul_f32_e32 v128, 0xbfb8aa3b, v126
	v_mul_f32_e32 v129, 0xbfb8aa3b, v127
	v_exp_f32_e32 v128, v128
	v_exp_f32_e32 v129, v129
	v_pk_mul_f32 v[102:103], v[102:103], v[162:163] op_sel_hi:[1,0]
	v_pk_mul_f32 v[98:99], v[98:99], v[162:163] op_sel_hi:[1,0]
	v_add_f32_e32 v128, 1.0, v128
	v_add_f32_e32 v129, 1.0, v129
	v_rcp_f32_e32 v128, v128
	v_rcp_f32_e32 v129, v129
	v_pk_mul_f32 v[100:101], v[100:101], v[162:163] op_sel_hi:[1,0]
	v_pk_mul_f32 v[94:95], v[94:95], v[158:159] op_sel_hi:[1,0]
	v_pk_mul_f32 v[90:91], v[90:91], v[158:159] op_sel_hi:[1,0]
	v_pk_mul_f32 v[126:127], v[126:127], v[128:129]
	v_pk_mul_f32 v[92:93], v[92:93], v[158:159] op_sel_hi:[1,0]
	v_pk_mul_f32 v[124:125], v[124:125], v[126:127]
	v_mul_f32_e32 v126, 0xbfb8aa3b, v118
	v_mul_f32_e32 v127, 0xbfb8aa3b, v119
	v_exp_f32_e32 v126, v126
	v_exp_f32_e32 v127, v127
	v_pk_mul_f32 v[86:87], v[86:87], v[158:159] op_sel_hi:[1,0]
	v_pk_mul_f32 v[82:83], v[82:83], v[158:159] op_sel_hi:[1,0]
	v_add_f32_e32 v126, 1.0, v126
	v_add_f32_e32 v127, 1.0, v127
	v_rcp_f32_e32 v126, v126
	v_rcp_f32_e32 v127, v127
	v_pk_mul_f32 v[84:85], v[84:85], v[158:159] op_sel_hi:[1,0]
	v_pk_mul_f32 v[78:79], v[78:79], v[156:157] op_sel_hi:[1,0]
	v_pk_mul_f32 v[74:75], v[74:75], v[156:157] op_sel_hi:[1,0]
	v_pk_mul_f32 v[118:119], v[118:119], v[126:127]
	v_pk_mul_f32 v[76:77], v[76:77], v[156:157] op_sel_hi:[1,0]
	v_pk_mul_f32 v[114:115], v[114:115], v[118:119]
	v_pk_mul_f32 v[118:119], v[120:121], v[164:165] op_sel_hi:[1,0]
	v_pk_mul_f32 v[70:71], v[70:71], v[156:157] op_sel_hi:[1,0]
	v_mul_f32_e32 v120, 0xbfb8aa3b, v118
	v_mul_f32_e32 v121, 0xbfb8aa3b, v119
	v_exp_f32_e32 v120, v120
	v_exp_f32_e32 v121, v121
	v_pk_mul_f32 v[66:67], v[66:67], v[156:157] op_sel_hi:[1,0]
	v_pk_mul_f32 v[68:69], v[68:69], v[156:157] op_sel_hi:[1,0]
	v_add_f32_e32 v120, 1.0, v120
	v_add_f32_e32 v121, 1.0, v121
	v_rcp_f32_e32 v120, v120
	v_rcp_f32_e32 v121, v121
	v_pk_mul_f32 v[62:63], v[62:63], v[140:141] op_sel_hi:[1,0]
	v_pk_mul_f32 v[58:59], v[58:59], v[140:141] op_sel_hi:[1,0]
	v_pk_mul_f32 v[60:61], v[60:61], v[140:141] op_sel_hi:[1,0]
	v_pk_mul_f32 v[118:119], v[118:119], v[120:121]
	v_pk_mul_f32 v[54:55], v[54:55], v[140:141] op_sel_hi:[1,0]
	v_pk_mul_f32 v[120:121], v[116:117], v[118:119]
	v_cvt_pk_bf16_f32 v118, v114, v115
	v_mul_f32_e32 v115, 0xbfb8aa3b, v110
	v_exp_f32_e32 v115, v115
	v_mul_lo_u32 v114, v160, s2
	v_cvt_pk_bf16_f32 v116, v122, v123
	v_cvt_pk_bf16_f32 v117, v124, v125
	v_cvt_pk_bf16_f32 v119, v120, v121
	v_add_lshl_u32 v114, v114, v168, 1
	v_add_f32_e32 v115, 1.0, v115
; __device__ __forceinline__ unsigned pk2(float lo, float hi) { const f32x2 f = {lo, hi}; const bf16n2 v = __builtin_convertvector(f, bf16n2); return __builtin_bit_cast(unsigned, v); }
; __device__ __forceinline__ float sigmoidf_(float x) { return __builtin_amdgcn_rcpf(1.0f + __expf(-x)); }
;     __device__ __forceinline__ bool operator()(f32x4 (&acc)[2][2][4][2], const Unit& u, int wr, int wc, int fr, int fq) const {
;     ...
;             for (int m = 0; m < 4; ++m) { const int row = row0 + ai * HALF + m * 16;
;                 const float s = sv[ai][m];
;                 float o[8];
; #pragma unroll
;                 for (int n = 0; n < 2; ++n)
; #pragma unroll
;                     for (int j = 0; j < 4; ++j) { const float gg = acc[ai][0][m][n][j] * s, uu = acc[ai][1][m][n][j] * s; o[n * 4 + j] = gg * sigmoidf_(gg) * uu; }
;                 u32x4 w; w.x = pk2(o[0], o[1]); w.y = pk2(o[2], o[3]); w.z = pk2(o[4], o[5]); w.w = pk2(o[6], o[7]);
;                 __builtin_amdgcn_raw_buffer_store_b128(w, rs_act, ((unsigned)row * (unsigned)FFN + (unsigned)col0) * 2u, 0, 0); }
	buffer_store_dwordx4 v[116:119], v114, s[8:11], 0 offen nt sc1
	v_pk_mul_f32 v[50:51], v[50:51], v[140:141] op_sel_hi:[1,0]
	v_pk_mul_f32 v[52:53], v[52:53], v[140:141] op_sel_hi:[1,0]
	v_rcp_f32_e32 v116, v115
	v_mul_f32_e32 v115, 0xbfb8aa3b, v111
	v_exp_f32_e32 v115, v115
	v_pk_mul_f32 v[46:47], v[46:47], v[138:139] op_sel_hi:[1,0]
	v_pk_mul_f32 v[42:43], v[42:43], v[138:139] op_sel_hi:[1,0]
	v_pk_mul_f32 v[44:45], v[44:45], v[138:139] op_sel_hi:[1,0]
	v_add_f32_e32 v115, 1.0, v115
	v_rcp_f32_e32 v117, v115
	v_pk_mul_f32 v[38:39], v[38:39], v[138:139] op_sel_hi:[1,0]
	v_pk_mul_f32 v[34:35], v[34:35], v[138:139] op_sel_hi:[1,0]
	v_pk_mul_f32 v[36:37], v[36:37], v[138:139] op_sel_hi:[1,0]
	v_pk_mul_f32 v[110:111], v[110:111], v[116:117]
	v_pk_mul_f32 v[30:31], v[30:31], v[132:133] op_sel_hi:[1,0]
	v_pk_mul_f32 v[106:107], v[106:107], v[110:111]
	v_pk_mul_f32 v[110:111], v[112:113], v[162:163] op_sel_hi:[1,0]
	v_pk_mul_f32 v[26:27], v[26:27], v[132:133] op_sel_hi:[1,0]
	v_mul_f32_e32 v112, 0xbfb8aa3b, v110
	v_mul_f32_e32 v113, 0xbfb8aa3b, v111
	v_exp_f32_e32 v112, v112
	v_exp_f32_e32 v113, v113
	v_pk_mul_f32 v[28:29], v[28:29], v[132:133] op_sel_hi:[1,0]
	v_pk_mul_f32 v[22:23], v[22:23], v[132:133] op_sel_hi:[1,0]
	v_add_f32_e32 v112, 1.0, v112
	v_add_f32_e32 v113, 1.0, v113
	v_rcp_f32_e32 v112, v112
	v_rcp_f32_e32 v113, v113
	v_pk_mul_f32 v[18:19], v[18:19], v[132:133] op_sel_hi:[1,0]
	v_pk_mul_f32 v[20:21], v[20:21], v[132:133] op_sel_hi:[1,0]
	v_pk_mul_f32 v[14:15], v[14:15], v[130:131] op_sel_hi:[1,0]
	v_pk_mul_f32 v[110:111], v[110:111], v[112:113]
	v_pk_mul_f32 v[10:11], v[10:11], v[130:131] op_sel_hi:[1,0]
	v_pk_mul_f32 v[108:109], v[108:109], v[110:111]
	v_mul_f32_e32 v110, 0xbfb8aa3b, v102
	v_mul_f32_e32 v111, 0xbfb8aa3b, v103
	v_exp_f32_e32 v110, v110
	v_exp_f32_e32 v111, v111
	v_pk_mul_f32 v[12:13], v[12:13], v[130:131] op_sel_hi:[1,0]
	v_pk_mul_f32 v[6:7], v[6:7], v[130:131] op_sel_hi:[1,0]
	v_add_f32_e32 v110, 1.0, v110
	v_add_f32_e32 v111, 1.0, v111
	v_rcp_f32_e32 v110, v110
	v_rcp_f32_e32 v111, v111
	v_pk_mul_f32 v[2:3], v[2:3], v[130:131] op_sel_hi:[1,0]
	s_mov_b64 s[48:49], s[8:9]
	v_pk_mul_f32 v[4:5], v[4:5], v[130:131] op_sel_hi:[1,0]
	v_pk_mul_f32 v[102:103], v[102:103], v[110:111]
	v_writelane_b32 v252, s48, 41
	v_pk_mul_f32 v[102:103], v[98:99], v[102:103]
	v_pk_mul_f32 v[98:99], v[104:105], v[162:163] op_sel_hi:[1,0]
	v_writelane_b32 v252, s49, 42
	v_mul_f32_e32 v104, 0xbfb8aa3b, v98
	v_mul_f32_e32 v105, 0xbfb8aa3b, v99
	v_exp_f32_e32 v104, v104
	v_exp_f32_e32 v105, v105
	v_writelane_b32 v252, s50, 43
	v_writelane_b32 v252, s51, 44
	v_add_f32_e32 v104, 1.0, v104
	v_add_f32_e32 v105, 1.0, v105
	v_rcp_f32_e32 v104, v104
	v_rcp_f32_e32 v105, v105
	s_and_b64 vcc, exec, s[0:1]
	s_mov_b64 s[2:3], s[4:5]
	v_pk_mul_f32 v[98:99], v[98:99], v[104:105]
	s_nop 0
	v_pk_mul_f32 v[104:105], v[100:101], v[98:99]
	v_cvt_pk_bf16_f32 v98, v106, v107
	v_cvt_pk_bf16_f32 v99, v108, v109
	v_cvt_pk_bf16_f32 v100, v102, v103
	v_cvt_pk_bf16_f32 v101, v104, v105
	v_add_u32_e32 v102, 0x16000, v114
	buffer_store_dwordx4 v[98:101], v102, s[8:11], 0 offen nt sc1
	s_nop 1
	v_mul_f32_e32 v98, 0xbfb8aa3b, v94
	v_mul_f32_e32 v99, 0xbfb8aa3b, v95
	v_exp_f32_e32 v98, v98
	v_exp_f32_e32 v99, v99
	v_add_f32_e32 v98, 1.0, v98
	v_add_f32_e32 v99, 1.0, v99
	v_rcp_f32_e32 v98, v98
	v_rcp_f32_e32 v99, v99
	s_nop 0
	v_pk_mul_f32 v[94:95], v[94:95], v[98:99]
	s_nop 0
	v_pk_mul_f32 v[90:91], v[90:91], v[94:95]
	v_pk_mul_f32 v[94:95], v[96:97], v[158:159] op_sel_hi:[1,0]
	s_nop 0
	v_mul_f32_e32 v96, 0xbfb8aa3b, v94
	v_mul_f32_e32 v97, 0xbfb8aa3b, v95
	v_exp_f32_e32 v96, v96
	v_exp_f32_e32 v97, v97
	v_add_f32_e32 v96, 1.0, v96
	v_add_f32_e32 v97, 1.0, v97
	v_rcp_f32_e32 v96, v96
	v_rcp_f32_e32 v97, v97
	s_nop 0
	v_pk_mul_f32 v[94:95], v[94:95], v[96:97]
	s_nop 0
	v_pk_mul_f32 v[92:93], v[92:93], v[94:95]
	v_mul_f32_e32 v94, 0xbfb8aa3b, v86
	v_mul_f32_e32 v95, 0xbfb8aa3b, v87
	v_exp_f32_e32 v94, v94
	v_exp_f32_e32 v95, v95
	v_add_f32_e32 v94, 1.0, v94
	v_add_f32_e32 v95, 1.0, v95
	v_rcp_f32_e32 v94, v94
	v_rcp_f32_e32 v95, v95
	s_nop 0
	v_pk_mul_f32 v[86:87], v[86:87], v[94:95]
	s_nop 0
	v_pk_mul_f32 v[86:87], v[82:83], v[86:87]
	v_pk_mul_f32 v[82:83], v[88:89], v[158:159] op_sel_hi:[1,0]
	s_nop 0
	v_mul_f32_e32 v88, 0xbfb8aa3b, v82
	v_mul_f32_e32 v89, 0xbfb8aa3b, v83
	v_exp_f32_e32 v88, v88
	v_exp_f32_e32 v89, v89
	v_add_f32_e32 v88, 1.0, v88
	v_add_f32_e32 v89, 1.0, v89
	v_rcp_f32_e32 v88, v88
	v_rcp_f32_e32 v89, v89
	s_nop 0
	v_pk_mul_f32 v[82:83], v[82:83], v[88:89]
	s_nop 0
	v_pk_mul_f32 v[88:89], v[84:85], v[82:83]
	v_cvt_pk_bf16_f32 v82, v90, v91
	v_cvt_pk_bf16_f32 v83, v92, v93
	v_cvt_pk_bf16_f32 v84, v86, v87
	v_cvt_pk_bf16_f32 v85, v88, v89
	v_add_u32_e32 v86, 0x2c000, v114
	buffer_store_dwordx4 v[82:85], v86, s[8:11], 0 offen nt sc1
	s_nop 1
	v_mul_f32_e32 v82, 0xbfb8aa3b, v78
	v_mul_f32_e32 v83, 0xbfb8aa3b, v79
	v_exp_f32_e32 v82, v82
	v_exp_f32_e32 v83, v83
	v_add_f32_e32 v82, 1.0, v82
	v_add_f32_e32 v83, 1.0, v83
	v_rcp_f32_e32 v82, v82
	v_rcp_f32_e32 v83, v83
	s_nop 0
	v_pk_mul_f32 v[78:79], v[78:79], v[82:83]
	s_nop 0
	v_pk_mul_f32 v[74:75], v[74:75], v[78:79]
	v_pk_mul_f32 v[78:79], v[80:81], v[156:157] op_sel_hi:[1,0]
	s_nop 0
	v_mul_f32_e32 v80, 0xbfb8aa3b, v78
	v_mul_f32_e32 v81, 0xbfb8aa3b, v79
	v_exp_f32_e32 v80, v80
	v_exp_f32_e32 v81, v81
	v_add_f32_e32 v80, 1.0, v80
	v_add_f32_e32 v81, 1.0, v81
	v_rcp_f32_e32 v80, v80
	v_rcp_f32_e32 v81, v81
	s_nop 0
	v_pk_mul_f32 v[78:79], v[78:79], v[80:81]
	s_nop 0
	v_pk_mul_f32 v[76:77], v[76:77], v[78:79]
	v_mul_f32_e32 v78, 0xbfb8aa3b, v70
	v_mul_f32_e32 v79, 0xbfb8aa3b, v71
	v_exp_f32_e32 v78, v78
; __device__ __forceinline__ unsigned pk2(float lo, float hi) { const f32x2 f = {lo, hi}; const bf16n2 v = __builtin_convertvector(f, bf16n2); return __builtin_bit_cast(unsigned, v); }
; __device__ __forceinline__ float sigmoidf_(float x) { return __builtin_amdgcn_rcpf(1.0f + __expf(-x)); }
;     __device__ __forceinline__ bool operator()(f32x4 (&acc)[2][2][4][2], const Unit& u, int wr, int wc, int fr, int fq) const {
;     ...
;             for (int m = 0; m < 4; ++m) { const int row = row0 + ai * HALF + m * 16;
;                 const float s = sv[ai][m];
;                 float o[8];
; #pragma unroll
;                 for (int n = 0; n < 2; ++n)
; #pragma unroll
;                     for (int j = 0; j < 4; ++j) { const float gg = acc[ai][0][m][n][j] * s, uu = acc[ai][1][m][n][j] * s; o[n * 4 + j] = gg * sigmoidf_(gg) * uu; }
;                 u32x4 w; w.x = pk2(o[0], o[1]); w.y = pk2(o[2], o[3]); w.z = pk2(o[4], o[5]); w.w = pk2(o[6], o[7]);
;                 __builtin_amdgcn_raw_buffer_store_b128(w, rs_act, ((unsigned)row * (unsigned)FFN + (unsigned)col0) * 2u, 0, 0); }
	v_exp_f32_e32 v79, v79
	v_add_f32_e32 v78, 1.0, v78
	v_add_f32_e32 v79, 1.0, v79
	v_rcp_f32_e32 v78, v78
	v_rcp_f32_e32 v79, v79
	s_nop 0
	v_pk_mul_f32 v[70:71], v[70:71], v[78:79]
	s_nop 0
	v_pk_mul_f32 v[70:71], v[66:67], v[70:71]
	v_pk_mul_f32 v[66:67], v[72:73], v[156:157] op_sel_hi:[1,0]
	s_nop 0
	v_mul_f32_e32 v72, 0xbfb8aa3b, v66
	v_mul_f32_e32 v73, 0xbfb8aa3b, v67
	v_exp_f32_e32 v72, v72
	v_exp_f32_e32 v73, v73
	v_add_f32_e32 v72, 1.0, v72
	v_add_f32_e32 v73, 1.0, v73
	v_rcp_f32_e32 v72, v72
	v_rcp_f32_e32 v73, v73
	s_nop 0
	v_pk_mul_f32 v[66:67], v[66:67], v[72:73]
	s_nop 0
	v_pk_mul_f32 v[72:73], v[68:69], v[66:67]
	v_cvt_pk_bf16_f32 v66, v74, v75
	v_cvt_pk_bf16_f32 v67, v76, v77
	v_cvt_pk_bf16_f32 v68, v70, v71
	v_cvt_pk_bf16_f32 v69, v72, v73
	v_add_u32_e32 v70, 0x42000, v114
	buffer_store_dwordx4 v[66:69], v70, s[8:11], 0 offen nt sc1
	s_nop 1
	v_mul_f32_e32 v66, 0xbfb8aa3b, v62
	v_mul_f32_e32 v67, 0xbfb8aa3b, v63
	v_exp_f32_e32 v66, v66
	v_exp_f32_e32 v67, v67
	v_add_f32_e32 v66, 1.0, v66
	v_add_f32_e32 v67, 1.0, v67
	v_rcp_f32_e32 v66, v66
	v_rcp_f32_e32 v67, v67
	s_nop 0
	v_pk_mul_f32 v[62:63], v[62:63], v[66:67]
	s_nop 0
	v_pk_mul_f32 v[58:59], v[58:59], v[62:63]
	v_pk_mul_f32 v[62:63], v[64:65], v[140:141] op_sel_hi:[1,0]
	s_nop 0
	v_mul_f32_e32 v64, 0xbfb8aa3b, v62
	v_mul_f32_e32 v65, 0xbfb8aa3b, v63
	v_exp_f32_e32 v64, v64
	v_exp_f32_e32 v65, v65
	v_add_f32_e32 v64, 1.0, v64
	v_add_f32_e32 v65, 1.0, v65
	v_rcp_f32_e32 v64, v64
	v_rcp_f32_e32 v65, v65
	s_nop 0
	v_pk_mul_f32 v[62:63], v[62:63], v[64:65]
	s_nop 0
	v_pk_mul_f32 v[60:61], v[60:61], v[62:63]
	v_mul_f32_e32 v62, 0xbfb8aa3b, v54
	v_mul_f32_e32 v63, 0xbfb8aa3b, v55
	v_exp_f32_e32 v62, v62
	v_exp_f32_e32 v63, v63
	v_add_f32_e32 v62, 1.0, v62
	v_add_f32_e32 v63, 1.0, v63
	v_rcp_f32_e32 v62, v62
	v_rcp_f32_e32 v63, v63
	s_nop 0
	v_pk_mul_f32 v[54:55], v[54:55], v[62:63]
	s_nop 0
	v_pk_mul_f32 v[54:55], v[50:51], v[54:55]
	v_pk_mul_f32 v[50:51], v[56:57], v[140:141] op_sel_hi:[1,0]
	s_nop 0
	v_mul_f32_e32 v56, 0xbfb8aa3b, v50
	v_mul_f32_e32 v57, 0xbfb8aa3b, v51
	v_exp_f32_e32 v56, v56
	v_exp_f32_e32 v57, v57
	v_add_f32_e32 v56, 1.0, v56
	v_add_f32_e32 v57, 1.0, v57
	v_rcp_f32_e32 v56, v56
	v_rcp_f32_e32 v57, v57
	s_nop 0
	v_pk_mul_f32 v[50:51], v[50:51], v[56:57]
	s_nop 0
	v_pk_mul_f32 v[56:57], v[52:53], v[50:51]
	v_cvt_pk_bf16_f32 v50, v58, v59
	v_cvt_pk_bf16_f32 v51, v60, v61
	v_cvt_pk_bf16_f32 v52, v54, v55
	v_cvt_pk_bf16_f32 v53, v56, v57
	v_add_u32_e32 v54, 0xb0000, v114
	buffer_store_dwordx4 v[50:53], v54, s[8:11], 0 offen nt sc1
	s_nop 1
	v_mul_f32_e32 v50, 0xbfb8aa3b, v46
	v_mul_f32_e32 v51, 0xbfb8aa3b, v47
	v_exp_f32_e32 v50, v50
	v_exp_f32_e32 v51, v51
	v_add_f32_e32 v50, 1.0, v50
	v_add_f32_e32 v51, 1.0, v51
	v_rcp_f32_e32 v50, v50
	v_rcp_f32_e32 v51, v51
	s_nop 0
	v_pk_mul_f32 v[46:47], v[46:47], v[50:51]
	s_nop 0
	v_pk_mul_f32 v[42:43], v[42:43], v[46:47]
	v_pk_mul_f32 v[46:47], v[48:49], v[138:139] op_sel_hi:[1,0]
	s_nop 0
	v_mul_f32_e32 v48, 0xbfb8aa3b, v46
	v_mul_f32_e32 v49, 0xbfb8aa3b, v47
	v_exp_f32_e32 v48, v48
	v_exp_f32_e32 v49, v49
	v_add_f32_e32 v48, 1.0, v48
	v_add_f32_e32 v49, 1.0, v49
	v_rcp_f32_e32 v48, v48
	v_rcp_f32_e32 v49, v49
	s_nop 0
	v_pk_mul_f32 v[46:47], v[46:47], v[48:49]
	s_nop 0
	v_pk_mul_f32 v[44:45], v[44:45], v[46:47]
	v_mul_f32_e32 v46, 0xbfb8aa3b, v38
	v_mul_f32_e32 v47, 0xbfb8aa3b, v39
	v_exp_f32_e32 v46, v46
	v_exp_f32_e32 v47, v47
	v_add_f32_e32 v46, 1.0, v46
	v_add_f32_e32 v47, 1.0, v47
	v_rcp_f32_e32 v46, v46
	v_rcp_f32_e32 v47, v47
	s_nop 0
	v_pk_mul_f32 v[38:39], v[38:39], v[46:47]
	s_nop 0
	v_pk_mul_f32 v[38:39], v[34:35], v[38:39]
	v_pk_mul_f32 v[34:35], v[40:41], v[138:139] op_sel_hi:[1,0]
	s_nop 0
	v_mul_f32_e32 v40, 0xbfb8aa3b, v34
	v_mul_f32_e32 v41, 0xbfb8aa3b, v35
	v_exp_f32_e32 v40, v40
	v_exp_f32_e32 v41, v41
	v_add_f32_e32 v40, 1.0, v40
	v_add_f32_e32 v41, 1.0, v41
; __device__ __forceinline__ unsigned pk2(float lo, float hi) { const f32x2 f = {lo, hi}; const bf16n2 v = __builtin_convertvector(f, bf16n2); return __builtin_bit_cast(unsigned, v); }
; __device__ __forceinline__ float sigmoidf_(float x) { return __builtin_amdgcn_rcpf(1.0f + __expf(-x)); }
; #define PG8_WAIT_V(n) asm volatile("s_waitcnt vmcnt(" #n ")" ::: "memory")
; template <class Epi>
; __device__ __forceinline__ void gemm_phase(LAS unsigned char* lds, const int tid, const Gemm g, const Sched& S, const Epi& E) {
;     ...
;         if (!has_next) break;
;         if (!keep) {
; #pragma unroll
;             for (int a = 0; a < 2; ++a)
; #pragma unroll
;                 for (int b = 0; b < 2; ++b)
; #pragma unroll
;                     for (int m = 0; m < 4; ++m)
; #pragma unroll
;                         for (int n = 0; n < 2; ++n) acc[a][b][m][n] = (f32x4){0.f, 0.f, 0.f, 0.f};
;         }
;         cur = nxt; cA = nA; cB = nB; ++ui;
;     }
;     PG8_WAIT_V(0);
;     __device__ __forceinline__ bool operator()(f32x4 (&acc)[2][2][4][2], const Unit& u, int wr, int wc, int fr, int fq) const {
;     ...
;             for (int m = 0; m < 4; ++m) { const int row = row0 + ai * HALF + m * 16;
;                 const float s = sv[ai][m];
;                 float o[8];
; #pragma unroll
;                 for (int n = 0; n < 2; ++n)
; #pragma unroll
;                     for (int j = 0; j < 4; ++j) { const float gg = acc[ai][0][m][n][j] * s, uu = acc[ai][1][m][n][j] * s; o[n * 4 + j] = gg * sigmoidf_(gg) * uu; }
;                 u32x4 w; w.x = pk2(o[0], o[1]); w.y = pk2(o[2], o[3]); w.z = pk2(o[4], o[5]); w.w = pk2(o[6], o[7]);
;                 __builtin_amdgcn_raw_buffer_store_b128(w, rs_act, ((unsigned)row * (unsigned)FFN + (unsigned)col0) * 2u, 0, 0); }
	v_rcp_f32_e32 v40, v40
	v_rcp_f32_e32 v41, v41
	s_nop 0
	v_pk_mul_f32 v[34:35], v[34:35], v[40:41]
	s_nop 0
	v_pk_mul_f32 v[40:41], v[36:37], v[34:35]
	v_cvt_pk_bf16_f32 v34, v42, v43
	v_cvt_pk_bf16_f32 v35, v44, v45
	v_cvt_pk_bf16_f32 v36, v38, v39
	v_cvt_pk_bf16_f32 v37, v40, v41
	v_add_u32_e32 v38, 0xc6000, v114
	buffer_store_dwordx4 v[34:37], v38, s[8:11], 0 offen nt sc1
	s_nop 1
	v_mul_f32_e32 v34, 0xbfb8aa3b, v30
	v_mul_f32_e32 v35, 0xbfb8aa3b, v31
	v_exp_f32_e32 v34, v34
	v_exp_f32_e32 v35, v35
	v_add_f32_e32 v34, 1.0, v34
	v_add_f32_e32 v35, 1.0, v35
	v_rcp_f32_e32 v34, v34
	v_rcp_f32_e32 v35, v35
	s_nop 0
	v_pk_mul_f32 v[30:31], v[30:31], v[34:35]
	s_nop 0
	v_pk_mul_f32 v[26:27], v[26:27], v[30:31]
	v_pk_mul_f32 v[30:31], v[32:33], v[132:133] op_sel_hi:[1,0]
	s_nop 0
	v_mul_f32_e32 v32, 0xbfb8aa3b, v30
	v_mul_f32_e32 v33, 0xbfb8aa3b, v31
	v_exp_f32_e32 v32, v32
	v_exp_f32_e32 v33, v33
	v_add_f32_e32 v32, 1.0, v32
	v_add_f32_e32 v33, 1.0, v33
	v_rcp_f32_e32 v32, v32
	v_rcp_f32_e32 v33, v33
	s_nop 0
	v_pk_mul_f32 v[30:31], v[30:31], v[32:33]
	s_nop 0
	v_pk_mul_f32 v[28:29], v[28:29], v[30:31]
	v_mul_f32_e32 v30, 0xbfb8aa3b, v22
	v_mul_f32_e32 v31, 0xbfb8aa3b, v23
	v_exp_f32_e32 v30, v30
	v_exp_f32_e32 v31, v31
	v_add_f32_e32 v30, 1.0, v30
	v_add_f32_e32 v31, 1.0, v31
	v_rcp_f32_e32 v30, v30
	v_rcp_f32_e32 v31, v31
	s_nop 0
	v_pk_mul_f32 v[22:23], v[22:23], v[30:31]
	s_nop 0
	v_pk_mul_f32 v[22:23], v[18:19], v[22:23]
	v_pk_mul_f32 v[18:19], v[24:25], v[132:133] op_sel_hi:[1,0]
	s_nop 0
	v_mul_f32_e32 v24, 0xbfb8aa3b, v18
	v_mul_f32_e32 v25, 0xbfb8aa3b, v19
	v_exp_f32_e32 v24, v24
	v_exp_f32_e32 v25, v25
	v_add_f32_e32 v24, 1.0, v24
	v_add_f32_e32 v25, 1.0, v25
	v_rcp_f32_e32 v24, v24
	v_rcp_f32_e32 v25, v25
	s_nop 0
	v_pk_mul_f32 v[18:19], v[18:19], v[24:25]
	s_nop 0
	v_pk_mul_f32 v[24:25], v[20:21], v[18:19]
	v_cvt_pk_bf16_f32 v18, v26, v27
	v_cvt_pk_bf16_f32 v19, v28, v29
	v_cvt_pk_bf16_f32 v20, v22, v23
	v_cvt_pk_bf16_f32 v21, v24, v25
	v_add_u32_e32 v22, 0xdc000, v114
	buffer_store_dwordx4 v[18:21], v22, s[8:11], 0 offen nt sc1
	s_nop 1
	v_mul_f32_e32 v18, 0xbfb8aa3b, v14
	v_mul_f32_e32 v19, 0xbfb8aa3b, v15
	v_exp_f32_e32 v18, v18
	v_exp_f32_e32 v19, v19
	v_add_f32_e32 v18, 1.0, v18
	v_add_f32_e32 v19, 1.0, v19
	v_rcp_f32_e32 v18, v18
	v_rcp_f32_e32 v19, v19
	s_nop 0
	v_pk_mul_f32 v[14:15], v[14:15], v[18:19]
	s_nop 0
	v_pk_mul_f32 v[10:11], v[10:11], v[14:15]
	v_pk_mul_f32 v[14:15], v[16:17], v[130:131] op_sel_hi:[1,0]
	s_nop 0
	v_mul_f32_e32 v16, 0xbfb8aa3b, v14
	v_mul_f32_e32 v17, 0xbfb8aa3b, v15
	v_exp_f32_e32 v16, v16
	v_exp_f32_e32 v17, v17
	v_add_f32_e32 v16, 1.0, v16
	v_add_f32_e32 v17, 1.0, v17
	v_rcp_f32_e32 v16, v16
	v_rcp_f32_e32 v17, v17
	s_nop 0
	v_pk_mul_f32 v[14:15], v[14:15], v[16:17]
	s_nop 0
	v_pk_mul_f32 v[12:13], v[12:13], v[14:15]
	v_mul_f32_e32 v14, 0xbfb8aa3b, v6
	v_mul_f32_e32 v15, 0xbfb8aa3b, v7
	v_exp_f32_e32 v14, v14
	v_exp_f32_e32 v15, v15
	v_add_f32_e32 v14, 1.0, v14
	v_add_f32_e32 v15, 1.0, v15
	v_rcp_f32_e32 v14, v14
	v_rcp_f32_e32 v15, v15
	s_nop 0
	v_pk_mul_f32 v[6:7], v[6:7], v[14:15]
	s_nop 0
	v_pk_mul_f32 v[6:7], v[2:3], v[6:7]
	v_pk_mul_f32 v[2:3], v[8:9], v[130:131] op_sel_hi:[1,0]
	s_nop 0
	v_mul_f32_e32 v8, 0xbfb8aa3b, v2
	v_mul_f32_e32 v9, 0xbfb8aa3b, v3
	v_exp_f32_e32 v8, v8
	v_exp_f32_e32 v9, v9
	v_add_f32_e32 v8, 1.0, v8
	v_add_f32_e32 v9, 1.0, v9
	v_rcp_f32_e32 v8, v8
	v_rcp_f32_e32 v9, v9
	s_nop 0
	v_pk_mul_f32 v[2:3], v[2:3], v[8:9]
	s_nop 0
	v_pk_mul_f32 v[8:9], v[4:5], v[2:3]
	v_cvt_pk_bf16_f32 v2, v10, v11
	v_cvt_pk_bf16_f32 v3, v12, v13
	v_cvt_pk_bf16_f32 v4, v6, v7
	v_cvt_pk_bf16_f32 v5, v8, v9
	v_add_u32_e32 v6, 0xf2000, v114
	buffer_store_dwordx4 v[2:5], v6, s[8:11], 0 offen nt sc1
	s_mov_b64 s[8:9], s[6:7]
	s_cbranch_vccz .LBB0_1601
	s_waitcnt vmcnt(0)
	s_cmpk_gt_u32 s13, 0xff
	s_cbranch_scc1 .LBB0_1608
	s_barrier
